# indexer step 1: loop unrolled 2x with current/next K-fragment register sets swapped (8 v_mov_b64 per tile removed) and histogram addresses from the packed key word in 4 instead of 5 VALU per pair
# speedup vs baseline: 1.0088x; 1.0036x over previous
.LBB0_382:
	s_cmp_eq_u32 s81, s0
	s_mov_b64 s[0:1], -1
	v_mfma_f32_32x32x16_bf16 v[10:25], v[80:83], v[84:87], 0
	v_mfma_f32_32x32x16_bf16 v[10:25], v[76:79], v[88:91], v[10:25]
	v_mfma_f32_32x32x16_bf16 v[10:25], v[72:75], v[92:95], v[10:25]
	v_mfma_f32_32x32x16_bf16 v[10:25], v[52:55], v[96:99], v[10:25]
	s_nop 11
	v_fma_f32 v48, |v10|, v2, 0
	v_fma_f32 v49, |v11|, v2, 0
	v_fma_f32 v50, |v12|, v2, 0
	v_fma_f32 v51, |v13|, v2, 0
	v_fma_f32 v212, |v14|, v2, 0
	v_fma_f32 v213, |v15|, v2, 0
	v_fma_f32 v215, |v16|, v2, 0
	v_fma_f32 v216, |v17|, v2, 0
	v_fma_f32 v217, |v18|, v2, 0
	v_fma_f32 v228, |v19|, v2, 0
	v_mfma_f32_32x32x16_bf16 v[4:19], v[80:83], v[100:103], 0
	v_fma_f32 v229, |v20|, v2, 0
	v_fma_f32 v230, |v21|, v2, 0
	v_mfma_f32_32x32x16_bf16 v[4:19], v[76:79], v[104:107], v[4:19]
	v_fma_f32 v234, |v22|, v2, 0
	v_fma_f32 v235, |v23|, v2, 0
	v_mfma_f32_32x32x16_bf16 v[4:19], v[72:75], v[108:111], v[4:19]
	v_fma_f32 v236, |v24|, v2, 0
	v_fma_f32 v237, |v25|, v2, 0
	v_mfma_f32_32x32x16_bf16 v[4:19], v[52:55], v[112:115], v[4:19]
	s_nop 11
	v_fma_f32 v48, |v4|, v249, v48
	v_mfma_f32_32x32x16_bf16 v[20:35], v[80:83], v[116:119], 0
	v_fma_f32 v49, |v5|, v249, v49
	v_fma_f32 v50, |v6|, v249, v50
	v_fma_f32 v51, |v7|, v249, v51
	v_mfma_f32_32x32x16_bf16 v[20:35], v[76:79], v[120:123], v[20:35]
	v_fma_f32 v8, |v8|, v249, v212
	v_fma_f32 v9, |v9|, v249, v213
	v_fma_f32 v10, |v10|, v249, v215
	v_fma_f32 v11, |v11|, v249, v216
	v_mfma_f32_32x32x16_bf16 v[20:35], v[72:75], v[124:127], v[20:35]
	v_fma_f32 v12, |v12|, v249, v217
	v_fma_f32 v13, |v13|, v249, v228
	v_fma_f32 v212, |v14|, v249, v229
	v_fma_f32 v213, |v15|, v249, v230
	v_fma_f32 v215, |v16|, v249, v234
	v_fma_f32 v216, |v17|, v249, v235
	v_fma_f32 v217, |v18|, v249, v236
	v_fma_f32 v228, |v19|, v249, v237
	v_mfma_f32_32x32x16_bf16 v[20:35], v[52:55], v[128:131], v[20:35]
	s_nop 11
	v_fma_f32 v24, |v24|, v250, v8
	v_fma_f32 v25, |v25|, v250, v9
	v_fma_f32 v26, |v26|, v250, v10
	v_fma_f32 v27, |v27|, v250, v11
	v_fma_f32 v28, |v28|, v250, v12
	v_fma_f32 v29, |v29|, v250, v13
	v_mfma_f32_32x32x16_bf16 v[4:19], v[80:83], v[132:135], 0
	v_fma_f32 v48, |v20|, v250, v48
	v_fma_f32 v49, |v21|, v250, v49
	v_fma_f32 v50, |v22|, v250, v50
	v_fma_f32 v51, |v23|, v250, v51
	v_mfma_f32_32x32x16_bf16 v[4:19], v[76:79], v[136:139], v[4:19]
	v_fma_f32 v212, |v30|, v250, v212
	v_mfma_f32_32x32x16_bf16 v[4:19], v[72:75], v[140:143], v[4:19]
	v_fma_f32 v213, |v31|, v250, v213
	v_fma_f32 v215, |v32|, v250, v215
	v_fma_f32 v216, |v33|, v250, v216
	v_fma_f32 v217, |v34|, v250, v217
	v_fma_f32 v228, |v35|, v250, v228
	v_mfma_f32_32x32x16_bf16 v[4:19], v[52:55], v[144:147], v[4:19]
	s_nop 11
	v_fma_f32 v229, |v8|, v251, v24
	v_fma_f32 v230, |v9|, v251, v25
	v_fma_f32 v234, |v10|, v251, v26
	v_fma_f32 v235, |v11|, v251, v27
	v_fma_f32 v236, |v12|, v251, v28
	v_fma_f32 v237, |v13|, v251, v29
	v_mfma_f32_32x32x16_bf16 v[20:35], v[80:83], v[148:151], 0
	v_fma_f32 v48, |v4|, v251, v48
	v_fma_f32 v49, |v5|, v251, v49
	v_fma_f32 v50, |v6|, v251, v50
	v_fma_f32 v51, |v7|, v251, v51
	v_mfma_f32_32x32x16_bf16 v[20:35], v[76:79], v[152:155], v[20:35]
	v_fma_f32 v212, |v14|, v251, v212
	v_mfma_f32_32x32x16_bf16 v[20:35], v[72:75], v[156:159], v[20:35]
	v_fma_f32 v213, |v15|, v251, v213
	v_fma_f32 v215, |v16|, v251, v215
	v_fma_f32 v216, |v17|, v251, v216
	v_fma_f32 v217, |v18|, v251, v217
	v_fma_f32 v228, |v19|, v251, v228
	v_mfma_f32_32x32x16_bf16 v[20:35], v[52:55], v[160:163], v[20:35]
	s_nop 11
	v_fma_f32 v20, |v20|, v252, v48
	v_fma_f32 v21, |v21|, v252, v49
	v_fma_f32 v22, |v22|, v252, v50
	v_fma_f32 v23, |v23|, v252, v51
	v_mfma_f32_32x32x16_bf16 v[36:51], v[80:83], v[164:167], 0
	v_fma_f32 v24, |v24|, v252, v229
	v_fma_f32 v25, |v25|, v252, v230
	v_mfma_f32_32x32x16_bf16 v[36:51], v[76:79], v[168:171], v[36:51]
	v_fma_f32 v26, |v26|, v252, v234
	v_fma_f32 v27, |v27|, v252, v235
	v_mfma_f32_32x32x16_bf16 v[36:51], v[72:75], v[172:175], v[36:51]
	v_fma_f32 v229, |v28|, v252, v236
	v_fma_f32 v230, |v29|, v252, v237
	v_fma_f32 v212, |v30|, v252, v212
	v_fma_f32 v213, |v31|, v252, v213
	v_fma_f32 v215, |v32|, v252, v215
	v_fma_f32 v216, |v33|, v252, v216
	v_fma_f32 v217, |v34|, v252, v217
	v_fma_f32 v228, |v35|, v252, v228
	v_mfma_f32_32x32x16_bf16 v[36:51], v[52:55], v[176:179], v[36:51]
	s_nop 11
	v_fma_f32 v234, |v36|, v253, v20
	v_fma_f32 v235, |v37|, v253, v21
	v_fma_f32 v236, |v38|, v253, v22
	v_fma_f32 v237, |v39|, v253, v23
	v_fma_f32 v40, |v40|, v253, v24
	v_fma_f32 v41, |v41|, v253, v25
	v_fma_f32 v42, |v42|, v253, v26
	v_fma_f32 v43, |v43|, v253, v27
	v_mfma_f32_32x32x16_bf16 v[12:27], v[80:83], v[180:183], 0
	v_fma_f32 v44, |v44|, v253, v229
	v_fma_f32 v45, |v45|, v253, v230
	v_mfma_f32_32x32x16_bf16 v[12:27], v[76:79], v[184:187], v[12:27]
	v_fma_f32 v46, |v46|, v253, v212
	v_fma_f32 v47, |v47|, v253, v213
	v_mfma_f32_32x32x16_bf16 v[12:27], v[72:75], v[188:191], v[12:27]
	v_fma_f32 v48, |v48|, v253, v215
	v_fma_f32 v49, |v49|, v253, v216
	v_fma_f32 v50, |v50|, v253, v217
	v_fma_f32 v51, |v51|, v253, v228
	v_mfma_f32_32x32x16_bf16 v[12:27], v[52:55], v[192:195], v[12:27]
	s_nop 11
	v_fma_f32 v212, |v12|, v223, v234
	v_fma_f32 v213, |v13|, v223, v235
	v_fma_f32 v215, |v14|, v223, v236
	v_fma_f32 v216, |v15|, v223, v237
	v_fma_f32 v217, |v16|, v223, v40
	v_fma_f32 v228, |v17|, v223, v41
	v_fma_f32 v229, |v18|, v223, v42
	v_fma_f32 v230, |v19|, v223, v43
	v_mfma_f32_32x32x16_bf16 v[4:19], v[80:83], v[196:199], 0
	v_fma_f32 v234, |v20|, v223, v44
	v_fma_f32 v235, |v21|, v223, v45
	v_mfma_f32_32x32x16_bf16 v[4:19], v[76:79], v[200:203], v[4:19]
	v_fma_f32 v236, |v22|, v223, v46
	v_fma_f32 v237, |v23|, v223, v47
	v_mfma_f32_32x32x16_bf16 v[4:19], v[72:75], v[204:207], v[4:19]
	v_fma_f32 v48, |v24|, v223, v48
	v_fma_f32 v49, |v25|, v223, v49
	v_fma_f32 v50, |v26|, v223, v50
	v_fma_f32 v51, |v27|, v223, v51
	v_mfma_f32_32x32x16_bf16 v[4:19], v[52:55], v[208:211], v[4:19]
	ds_read_b128 v[20:23], v214 offset:32768
	ds_read_b128 v[36:39], v214 offset:33792
	ds_read_b128 v[40:43], v214 offset:34816
	ds_read_b128 v[44:47], v214 offset:35840
	s_waitcnt lgkmcnt(3)
	v_mfma_f32_32x32x16_bf16 v[20:35], v[80:83], v[20:23], 0
	s_nop 5
	v_fma_f32 v212, |v4|, v219, v212
	v_fma_f32 v213, |v5|, v219, v213
	v_fma_f32 v4, |v6|, v219, v215
	v_fma_f32 v5, |v7|, v219, v216
	s_waitcnt lgkmcnt(2)
	v_mfma_f32_32x32x16_bf16 v[20:35], v[76:79], v[36:39], v[20:35]
	v_fma_f32 v6, |v8|, v219, v217
	v_fma_f32 v7, |v9|, v219, v228
	v_fma_f32 v8, |v10|, v219, v229
	v_fma_f32 v9, |v11|, v219, v230
	s_waitcnt lgkmcnt(1)
	v_mfma_f32_32x32x16_bf16 v[20:35], v[72:75], v[40:43], v[20:35]
	v_fma_f32 v36, |v12|, v219, v234
	v_fma_f32 v37, |v13|, v219, v235
	v_fma_f32 v38, |v14|, v219, v236
	v_fma_f32 v39, |v15|, v219, v237
	s_waitcnt lgkmcnt(0)
	v_mfma_f32_32x32x16_bf16 v[20:35], v[52:55], v[44:47], v[20:35]
	v_fma_f32 v16, |v16|, v219, v48
	v_fma_f32 v17, |v17|, v219, v49
	s_nop 9
	v_add_f32_e32 v20, v212, v20
	v_pk_add_f32 v[14:15], v[4:5], v[22:23]
	v_pk_add_f32 v[4:5], v[32:33], v[16:17]
	v_cvt_f16_f32_e32 v16, v20
	v_fma_f32 v18, |v18|, v219, v50
	v_fma_f32 v19, |v19|, v219, v51
	v_add_f32_e32 v21, v213, v21
	v_add_f32_e32 v17, v34, v18
	v_add_f32_e32 v19, v35, v19
	v_bitop3_b32 v18, v16, s7, v16 bitop3:0xc
	v_or_b32_e32 v20, 0x8000, v16
	v_cmp_gt_i16_e32 vcc, 0, v16
	v_pk_add_f32 v[10:11], v[8:9], v[26:27]
	v_pk_add_f32 v[8:9], v[36:37], v[28:29]
	v_cndmask_b32_e32 v26, v20, v18, vcc
	v_cvt_f16_f32_e32 v29, v21
	v_cvt_f16_f32_e32 v18, v17
	v_cvt_f16_f32_e32 v17, v19
	v_pk_add_f32 v[12:13], v[6:7], v[24:25]
	v_pk_add_f32 v[6:7], v[38:39], v[30:31]
	v_bitop3_b32 v30, v29, s7, v29 bitop3:0xc
	v_or_b32_e32 v31, 0x8000, v29
	v_cmp_gt_i16_e64 s[60:61], 0, v29
	v_bitop3_b32 v21, v18, s7, v18 bitop3:0xc
	v_or_b32_e32 v22, 0x8000, v18
	v_cmp_gt_i16_e64 s[58:59], 0, v18
	v_bitop3_b32 v19, v17, s7, v17 bitop3:0xc
	v_or_b32_e32 v20, 0x8000, v17
	v_cmp_gt_i16_e32 vcc, 0, v17
	s_cbranch_scc1 .LBB0_384
	v_bfe_u32 v16, v26, 8, 8
	v_lshl_add_u32 v16, v16, 2, v222
	ds_add_u32 v16, v224 offset:36864
	v_cndmask_b32_e64 v16, v31, v30, s[60:61]
	v_cndmask_b32_e32 v40, v20, v19, vcc
	v_cndmask_b32_e64 v38, v22, v21, s[58:59]
	v_bfe_u32 v23, v16, 8, 8
	v_lshl_add_u32 v23, v23, 2, v222
	ds_add_u32 v23, v224 offset:36864
	v_lshrrev_b32_e32 v41, 8, v40
	v_bfe_u32 v24, v38, 8, 8
	v_lshl_add_u32 v24, v24, 2, v222
	ds_add_u32 v24, v224 offset:36864
	s_mov_b64 s[0:1], 0
	v_cvt_pk_f16_f32 v23, v6, v7
	v_pk_ashrrev_i16 v24, 15, v23 op_sel_hi:[0,1]
	v_bitop3_b32 v7, v23, v24, s32 bitop3:0x1e
	v_bfe_u32 v24, v7, 8, 8
	v_lshrrev_b32_e32 v23, 24, v7
	v_lshl_add_u32 v24, v24, 2, v222
	v_lshl_add_u32 v23, v23, 2, v222
	ds_add_u32 v24, v224 offset:36864
	ds_add_u32 v23, v224 offset:36864
	v_cvt_pk_f16_f32 v25, v8, v9
	v_pk_ashrrev_i16 v27, 15, v25 op_sel_hi:[0,1]
	v_bitop3_b32 v6, v25, v27, s32 bitop3:0x1e
	v_bfe_u32 v27, v6, 8, 8
	v_lshrrev_b32_e32 v25, 24, v6
	v_lshl_add_u32 v27, v27, 2, v222
	v_lshl_add_u32 v25, v25, 2, v222
	ds_add_u32 v27, v224 offset:36864
	ds_add_u32 v25, v224 offset:36864
	v_cvt_pk_f16_f32 v28, v10, v11
	v_pk_ashrrev_i16 v32, 15, v28 op_sel_hi:[0,1]
	v_bitop3_b32 v9, v28, v32, s32 bitop3:0x1e
	v_bfe_u32 v32, v9, 8, 8
	v_lshrrev_b32_e32 v28, 24, v9
	v_lshl_add_u32 v32, v32, 2, v222
	v_lshl_add_u32 v28, v28, 2, v222
	ds_add_u32 v32, v224 offset:36864
	ds_add_u32 v28, v224 offset:36864
	v_cvt_pk_f16_f32 v33, v12, v13
	v_pk_ashrrev_i16 v34, 15, v33 op_sel_hi:[0,1]
	v_bitop3_b32 v8, v33, v34, s32 bitop3:0x1e
	v_bfe_u32 v34, v8, 8, 8
	v_lshrrev_b32_e32 v33, 24, v8
	v_lshl_add_u32 v34, v34, 2, v222
	v_lshl_add_u32 v33, v33, 2, v222
	ds_add_u32 v34, v224 offset:36864
	ds_add_u32 v33, v224 offset:36864
	v_cvt_pk_f16_f32 v35, v4, v5
	v_pk_ashrrev_i16 v36, 15, v35 op_sel_hi:[0,1]
	v_bitop3_b32 v10, v35, v36, s32 bitop3:0x1e
	v_bfe_u32 v36, v10, 8, 8
	v_lshrrev_b32_e32 v35, 24, v10
	v_lshl_add_u32 v36, v36, 2, v222
	v_lshl_add_u32 v35, v35, 2, v222
	ds_add_u32 v36, v224 offset:36864
	ds_add_u32 v35, v224 offset:36864
	v_cvt_pk_f16_f32 v37, v14, v15
	v_pk_ashrrev_i16 v39, 15, v37 op_sel_hi:[0,1]
	v_bitop3_b32 v5, v37, v39, s32 bitop3:0x1e
	v_bfe_u32 v39, v5, 8, 8
	v_lshrrev_b32_e32 v37, 24, v5
	v_lshl_add_u32 v39, v39, 2, v222
	v_lshl_add_u32 v37, v37, 2, v222
	ds_add_u32 v39, v224 offset:36864
	ds_add_u32 v37, v224 offset:36864
	v_lshl_add_u32 v42, v41, 2, v222
	ds_add_u32 v42, v224 offset:36864
	v_lshl_or_b32 v4, v16, 16, v26
	v_lshl_or_b32 v11, v40, 16, v38
	s_nop 1
	s_branch .Lidx_join

.Lidx_join:
	v_permlane32_swap_b32_e32 v4, v6
	v_permlane32_swap_b32_e32 v5, v7
	v_permlane32_swap_b32_e32 v8, v10
	v_permlane32_swap_b32_e32 v9, v11
	s_and_b64 vcc, exec, s[18:19]
	global_store_dwordx4 v231, v[4:7], s[12:13]
	global_store_dwordx4 v231, v[8:11], s[12:13] offset:16
	v_add_u32_e32 v231, 0x4000, v231
	s_addk_i32 s95, 0x100
	s_cbranch_vccnz .LBB0_390
	s_waitcnt vmcnt(2)
	s_mov_b32 s0, s79
	s_branch .Lst_380
.Lst_380:
	s_add_i32 s79, s0, 8
	s_cmp_gt_i32 s79, s81
	s_cselect_b64 s[18:19], -1, 0
	s_cbranch_scc1 .Lst_382
	v_mad_i64_i32 v[4:5], s[58:59], s95, v240, v[220:221]
	global_load_dwordx4 v[80:83], v[4:5], off offset:3328
	global_load_dwordx4 v[76:79], v[4:5], off offset:3360
	global_load_dwordx4 v[72:75], v[4:5], off offset:3392
	global_load_dwordx4 v[52:55], v[4:5], off offset:3424
.Lst_382:
	s_cmp_eq_u32 s81, s0
	s_mov_b64 s[0:1], -1
	v_mfma_f32_32x32x16_bf16 v[10:25], v[68:71], v[84:87], 0
	v_mfma_f32_32x32x16_bf16 v[10:25], v[64:67], v[88:91], v[10:25]
	v_mfma_f32_32x32x16_bf16 v[10:25], v[60:63], v[92:95], v[10:25]
	v_mfma_f32_32x32x16_bf16 v[10:25], v[56:59], v[96:99], v[10:25]
	s_nop 11
	v_fma_f32 v48, |v10|, v2, 0
	v_fma_f32 v49, |v11|, v2, 0
	v_fma_f32 v50, |v12|, v2, 0
	v_fma_f32 v51, |v13|, v2, 0
	v_fma_f32 v212, |v14|, v2, 0
	v_fma_f32 v213, |v15|, v2, 0
	v_fma_f32 v215, |v16|, v2, 0
	v_fma_f32 v216, |v17|, v2, 0
	v_fma_f32 v217, |v18|, v2, 0
	v_fma_f32 v228, |v19|, v2, 0
	v_mfma_f32_32x32x16_bf16 v[4:19], v[68:71], v[100:103], 0
	v_fma_f32 v229, |v20|, v2, 0
	v_fma_f32 v230, |v21|, v2, 0
	v_mfma_f32_32x32x16_bf16 v[4:19], v[64:67], v[104:107], v[4:19]
	v_fma_f32 v234, |v22|, v2, 0
	v_fma_f32 v235, |v23|, v2, 0
	v_mfma_f32_32x32x16_bf16 v[4:19], v[60:63], v[108:111], v[4:19]
	v_fma_f32 v236, |v24|, v2, 0
	v_fma_f32 v237, |v25|, v2, 0
	v_mfma_f32_32x32x16_bf16 v[4:19], v[56:59], v[112:115], v[4:19]
	s_nop 11
	v_fma_f32 v48, |v4|, v249, v48
	v_mfma_f32_32x32x16_bf16 v[20:35], v[68:71], v[116:119], 0
	v_fma_f32 v49, |v5|, v249, v49
	v_fma_f32 v50, |v6|, v249, v50
	v_fma_f32 v51, |v7|, v249, v51
	v_mfma_f32_32x32x16_bf16 v[20:35], v[64:67], v[120:123], v[20:35]
	v_fma_f32 v8, |v8|, v249, v212
	v_fma_f32 v9, |v9|, v249, v213
	v_fma_f32 v10, |v10|, v249, v215
	v_fma_f32 v11, |v11|, v249, v216
	v_mfma_f32_32x32x16_bf16 v[20:35], v[60:63], v[124:127], v[20:35]
	v_fma_f32 v12, |v12|, v249, v217
	v_fma_f32 v13, |v13|, v249, v228
	v_fma_f32 v212, |v14|, v249, v229
	v_fma_f32 v213, |v15|, v249, v230
	v_fma_f32 v215, |v16|, v249, v234
	v_fma_f32 v216, |v17|, v249, v235
	v_fma_f32 v217, |v18|, v249, v236
	v_fma_f32 v228, |v19|, v249, v237
	v_mfma_f32_32x32x16_bf16 v[20:35], v[56:59], v[128:131], v[20:35]
	s_nop 11
	v_fma_f32 v24, |v24|, v250, v8
	v_fma_f32 v25, |v25|, v250, v9
	v_fma_f32 v26, |v26|, v250, v10
	v_fma_f32 v27, |v27|, v250, v11
	v_fma_f32 v28, |v28|, v250, v12
	v_fma_f32 v29, |v29|, v250, v13
	v_mfma_f32_32x32x16_bf16 v[4:19], v[68:71], v[132:135], 0
	v_fma_f32 v48, |v20|, v250, v48
	v_fma_f32 v49, |v21|, v250, v49
	v_fma_f32 v50, |v22|, v250, v50
	v_fma_f32 v51, |v23|, v250, v51
	v_mfma_f32_32x32x16_bf16 v[4:19], v[64:67], v[136:139], v[4:19]
	v_fma_f32 v212, |v30|, v250, v212
	v_mfma_f32_32x32x16_bf16 v[4:19], v[60:63], v[140:143], v[4:19]
	v_fma_f32 v213, |v31|, v250, v213
	v_fma_f32 v215, |v32|, v250, v215
	v_fma_f32 v216, |v33|, v250, v216
	v_fma_f32 v217, |v34|, v250, v217
	v_fma_f32 v228, |v35|, v250, v228
	v_mfma_f32_32x32x16_bf16 v[4:19], v[56:59], v[144:147], v[4:19]
	s_nop 11
	v_fma_f32 v229, |v8|, v251, v24
	v_fma_f32 v230, |v9|, v251, v25
	v_fma_f32 v234, |v10|, v251, v26
	v_fma_f32 v235, |v11|, v251, v27
	v_fma_f32 v236, |v12|, v251, v28
	v_fma_f32 v237, |v13|, v251, v29
	v_mfma_f32_32x32x16_bf16 v[20:35], v[68:71], v[148:151], 0
	v_fma_f32 v48, |v4|, v251, v48
	v_fma_f32 v49, |v5|, v251, v49
	v_fma_f32 v50, |v6|, v251, v50
	v_fma_f32 v51, |v7|, v251, v51
	v_mfma_f32_32x32x16_bf16 v[20:35], v[64:67], v[152:155], v[20:35]
	v_fma_f32 v212, |v14|, v251, v212
	v_mfma_f32_32x32x16_bf16 v[20:35], v[60:63], v[156:159], v[20:35]
	v_fma_f32 v213, |v15|, v251, v213
	v_fma_f32 v215, |v16|, v251, v215
	v_fma_f32 v216, |v17|, v251, v216
	v_fma_f32 v217, |v18|, v251, v217
	v_fma_f32 v228, |v19|, v251, v228
	v_mfma_f32_32x32x16_bf16 v[20:35], v[56:59], v[160:163], v[20:35]
	s_nop 11
	v_fma_f32 v20, |v20|, v252, v48
	v_fma_f32 v21, |v21|, v252, v49
	v_fma_f32 v22, |v22|, v252, v50
	v_fma_f32 v23, |v23|, v252, v51
	v_mfma_f32_32x32x16_bf16 v[36:51], v[68:71], v[164:167], 0
	v_fma_f32 v24, |v24|, v252, v229
	v_fma_f32 v25, |v25|, v252, v230
	v_mfma_f32_32x32x16_bf16 v[36:51], v[64:67], v[168:171], v[36:51]
	v_fma_f32 v26, |v26|, v252, v234
	v_fma_f32 v27, |v27|, v252, v235
	v_mfma_f32_32x32x16_bf16 v[36:51], v[60:63], v[172:175], v[36:51]
	v_fma_f32 v229, |v28|, v252, v236
	v_fma_f32 v230, |v29|, v252, v237
	v_fma_f32 v212, |v30|, v252, v212
	v_fma_f32 v213, |v31|, v252, v213
	v_fma_f32 v215, |v32|, v252, v215
	v_fma_f32 v216, |v33|, v252, v216
	v_fma_f32 v217, |v34|, v252, v217
	v_fma_f32 v228, |v35|, v252, v228
	v_mfma_f32_32x32x16_bf16 v[36:51], v[56:59], v[176:179], v[36:51]
	s_nop 11
	v_fma_f32 v234, |v36|, v253, v20
	v_fma_f32 v235, |v37|, v253, v21
	v_fma_f32 v236, |v38|, v253, v22
	v_fma_f32 v237, |v39|, v253, v23
	v_fma_f32 v40, |v40|, v253, v24
	v_fma_f32 v41, |v41|, v253, v25
	v_fma_f32 v42, |v42|, v253, v26
	v_fma_f32 v43, |v43|, v253, v27
	v_mfma_f32_32x32x16_bf16 v[12:27], v[68:71], v[180:183], 0
	v_fma_f32 v44, |v44|, v253, v229
	v_fma_f32 v45, |v45|, v253, v230
	v_mfma_f32_32x32x16_bf16 v[12:27], v[64:67], v[184:187], v[12:27]
	v_fma_f32 v46, |v46|, v253, v212
	v_fma_f32 v47, |v47|, v253, v213
	v_mfma_f32_32x32x16_bf16 v[12:27], v[60:63], v[188:191], v[12:27]
	v_fma_f32 v48, |v48|, v253, v215
	v_fma_f32 v49, |v49|, v253, v216
	v_fma_f32 v50, |v50|, v253, v217
	v_fma_f32 v51, |v51|, v253, v228
	v_mfma_f32_32x32x16_bf16 v[12:27], v[56:59], v[192:195], v[12:27]
	s_nop 11
	v_fma_f32 v212, |v12|, v223, v234
	v_fma_f32 v213, |v13|, v223, v235
	v_fma_f32 v215, |v14|, v223, v236
	v_fma_f32 v216, |v15|, v223, v237
	v_fma_f32 v217, |v16|, v223, v40
	v_fma_f32 v228, |v17|, v223, v41
	v_fma_f32 v229, |v18|, v223, v42
	v_fma_f32 v230, |v19|, v223, v43
	v_mfma_f32_32x32x16_bf16 v[4:19], v[68:71], v[196:199], 0
	v_fma_f32 v234, |v20|, v223, v44
	v_fma_f32 v235, |v21|, v223, v45
	v_mfma_f32_32x32x16_bf16 v[4:19], v[64:67], v[200:203], v[4:19]
	v_fma_f32 v236, |v22|, v223, v46
	v_fma_f32 v237, |v23|, v223, v47
	v_mfma_f32_32x32x16_bf16 v[4:19], v[60:63], v[204:207], v[4:19]
	v_fma_f32 v48, |v24|, v223, v48
	v_fma_f32 v49, |v25|, v223, v49
	v_fma_f32 v50, |v26|, v223, v50
	v_fma_f32 v51, |v27|, v223, v51
	v_mfma_f32_32x32x16_bf16 v[4:19], v[56:59], v[208:211], v[4:19]
	ds_read_b128 v[20:23], v214 offset:32768
	ds_read_b128 v[36:39], v214 offset:33792
	ds_read_b128 v[40:43], v214 offset:34816
	ds_read_b128 v[44:47], v214 offset:35840
	s_waitcnt lgkmcnt(3)
	v_mfma_f32_32x32x16_bf16 v[20:35], v[68:71], v[20:23], 0
	s_nop 5
	v_fma_f32 v212, |v4|, v219, v212
	v_fma_f32 v213, |v5|, v219, v213
	v_fma_f32 v4, |v6|, v219, v215
	v_fma_f32 v5, |v7|, v219, v216
	s_waitcnt lgkmcnt(2)
	v_mfma_f32_32x32x16_bf16 v[20:35], v[64:67], v[36:39], v[20:35]
	v_fma_f32 v6, |v8|, v219, v217
	v_fma_f32 v7, |v9|, v219, v228
	v_fma_f32 v8, |v10|, v219, v229
	v_fma_f32 v9, |v11|, v219, v230
	s_waitcnt lgkmcnt(1)
	v_mfma_f32_32x32x16_bf16 v[20:35], v[60:63], v[40:43], v[20:35]
	v_fma_f32 v36, |v12|, v219, v234
	v_fma_f32 v37, |v13|, v219, v235
	v_fma_f32 v38, |v14|, v219, v236
	v_fma_f32 v39, |v15|, v219, v237
	s_waitcnt lgkmcnt(0)
	v_mfma_f32_32x32x16_bf16 v[20:35], v[56:59], v[44:47], v[20:35]
	v_fma_f32 v16, |v16|, v219, v48
	v_fma_f32 v17, |v17|, v219, v49
	s_nop 9
	v_add_f32_e32 v20, v212, v20
	v_pk_add_f32 v[14:15], v[4:5], v[22:23]
	v_pk_add_f32 v[4:5], v[32:33], v[16:17]
	v_cvt_f16_f32_e32 v16, v20
	v_fma_f32 v18, |v18|, v219, v50
	v_fma_f32 v19, |v19|, v219, v51
	v_add_f32_e32 v21, v213, v21
	v_add_f32_e32 v17, v34, v18
	v_add_f32_e32 v19, v35, v19
	v_bitop3_b32 v18, v16, s7, v16 bitop3:0xc
	v_or_b32_e32 v20, 0x8000, v16
	v_cmp_gt_i16_e32 vcc, 0, v16
	v_pk_add_f32 v[10:11], v[8:9], v[26:27]
	v_pk_add_f32 v[8:9], v[36:37], v[28:29]
	v_cndmask_b32_e32 v26, v20, v18, vcc
	v_cvt_f16_f32_e32 v29, v21
	v_cvt_f16_f32_e32 v18, v17
	v_cvt_f16_f32_e32 v17, v19
	v_pk_add_f32 v[12:13], v[6:7], v[24:25]
	v_pk_add_f32 v[6:7], v[38:39], v[30:31]
	v_bitop3_b32 v30, v29, s7, v29 bitop3:0xc
	v_or_b32_e32 v31, 0x8000, v29
	v_cmp_gt_i16_e64 s[60:61], 0, v29
	v_bitop3_b32 v21, v18, s7, v18 bitop3:0xc
	v_or_b32_e32 v22, 0x8000, v18
	v_cmp_gt_i16_e64 s[58:59], 0, v18
	v_bitop3_b32 v19, v17, s7, v17 bitop3:0xc
	v_or_b32_e32 v20, 0x8000, v17
	v_cmp_gt_i16_e32 vcc, 0, v17
	s_cbranch_scc1 .Lst_384
	v_bfe_u32 v16, v26, 8, 8
	v_lshl_add_u32 v16, v16, 2, v222
	ds_add_u32 v16, v224 offset:36864
	v_cndmask_b32_e64 v16, v31, v30, s[60:61]
	v_cndmask_b32_e32 v40, v20, v19, vcc
	v_cndmask_b32_e64 v38, v22, v21, s[58:59]
	v_bfe_u32 v23, v16, 8, 8
	v_lshl_add_u32 v23, v23, 2, v222
	ds_add_u32 v23, v224 offset:36864
	v_lshrrev_b32_e32 v41, 8, v40
	v_bfe_u32 v24, v38, 8, 8
	v_lshl_add_u32 v24, v24, 2, v222
	ds_add_u32 v24, v224 offset:36864
	s_mov_b64 s[0:1], 0
	v_cvt_pk_f16_f32 v23, v6, v7
	v_pk_ashrrev_i16 v24, 15, v23 op_sel_hi:[0,1]
	v_bitop3_b32 v7, v23, v24, s32 bitop3:0x1e
	v_bfe_u32 v24, v7, 8, 8
	v_lshrrev_b32_e32 v23, 24, v7
	v_lshl_add_u32 v24, v24, 2, v222
	v_lshl_add_u32 v23, v23, 2, v222
	ds_add_u32 v24, v224 offset:36864
	ds_add_u32 v23, v224 offset:36864
	v_cvt_pk_f16_f32 v25, v8, v9
	v_pk_ashrrev_i16 v27, 15, v25 op_sel_hi:[0,1]
	v_bitop3_b32 v6, v25, v27, s32 bitop3:0x1e
	v_bfe_u32 v27, v6, 8, 8
	v_lshrrev_b32_e32 v25, 24, v6
	v_lshl_add_u32 v27, v27, 2, v222
	v_lshl_add_u32 v25, v25, 2, v222
	ds_add_u32 v27, v224 offset:36864
	ds_add_u32 v25, v224 offset:36864
	v_cvt_pk_f16_f32 v28, v10, v11
	v_pk_ashrrev_i16 v32, 15, v28 op_sel_hi:[0,1]
	v_bitop3_b32 v9, v28, v32, s32 bitop3:0x1e
	v_bfe_u32 v32, v9, 8, 8
	v_lshrrev_b32_e32 v28, 24, v9
	v_lshl_add_u32 v32, v32, 2, v222
	v_lshl_add_u32 v28, v28, 2, v222
	ds_add_u32 v32, v224 offset:36864
	ds_add_u32 v28, v224 offset:36864
	v_cvt_pk_f16_f32 v33, v12, v13
	v_pk_ashrrev_i16 v34, 15, v33 op_sel_hi:[0,1]
	v_bitop3_b32 v8, v33, v34, s32 bitop3:0x1e
	v_bfe_u32 v34, v8, 8, 8
	v_lshrrev_b32_e32 v33, 24, v8
	v_lshl_add_u32 v34, v34, 2, v222
	v_lshl_add_u32 v33, v33, 2, v222
	ds_add_u32 v34, v224 offset:36864
	ds_add_u32 v33, v224 offset:36864
	v_cvt_pk_f16_f32 v35, v4, v5
	v_pk_ashrrev_i16 v36, 15, v35 op_sel_hi:[0,1]
	v_bitop3_b32 v10, v35, v36, s32 bitop3:0x1e
	v_bfe_u32 v36, v10, 8, 8
	v_lshrrev_b32_e32 v35, 24, v10
	v_lshl_add_u32 v36, v36, 2, v222
	v_lshl_add_u32 v35, v35, 2, v222
	ds_add_u32 v36, v224 offset:36864
	ds_add_u32 v35, v224 offset:36864
	v_cvt_pk_f16_f32 v37, v14, v15
	v_pk_ashrrev_i16 v39, 15, v37 op_sel_hi:[0,1]
	v_bitop3_b32 v5, v37, v39, s32 bitop3:0x1e
	v_bfe_u32 v39, v5, 8, 8
	v_lshrrev_b32_e32 v37, 24, v5
	v_lshl_add_u32 v39, v39, 2, v222
	v_lshl_add_u32 v37, v37, 2, v222
	ds_add_u32 v39, v224 offset:36864
	ds_add_u32 v37, v224 offset:36864
	v_lshl_add_u32 v42, v41, 2, v222
	ds_add_u32 v42, v224 offset:36864
	v_lshl_or_b32 v4, v16, 16, v26
	v_lshl_or_b32 v11, v40, 16, v38
	s_nop 1
	s_branch .Lidx_join_b
